# speedup vs baseline: 1.0431x; 1.0004x over previous
.LBB2_114:
	s_setprio 0
	v_and_b32_e32 v0, 16, v0
	v_lshlrev_b32_e32 v1, 2, v191
	s_lshl_b32 s0, s34, 5
	v_add_u32_e32 v70, 12, v1
	v_cmp_eq_u32_e32 vcc, 0, v0
	s_add_i32 s0, s0, s33
	s_mov_b32 s1, 0x3f3504f3
	v_cndmask_b32_e32 v0, v70, v1, vcc
	v_or_b32_e32 v0, s0, v0
	v_ashrrev_i32_e32 v1, 31, v0
	v_lshl_add_u64 v[78:79], v[0:1], 1, s[4:5]
	s_waitcnt vmcnt(0) lgkmcnt(0)
	s_mov_b32 s76, 0x3e6d3388
	s_mov_b32 s78, 0xbf38aa3b
	s_mov_b32 s80, 0x3f87dc22
	s_mov_b32 s82, 0x3fb5f0e3
	s_mov_b32 s84, 0xbe91a98e
	s_mov_b32 s86, 0x3e827906
	v_mov_b32_e32 v248, 0xbfba00e3
	v_mov_b32_e32 v249, 0xbfba00e3
	v_mul_f32_e32 v232, 0.5, v220
	v_pk_mul_f32 v[234:235], v[74:75], v[74:75]
	v_pk_mul_f32 v[252:253], v[76:77], v[76:77]
	v_fma_f32 v236, |v74|, s76, 1.0
	v_fma_f32 v254, |v76|, s76, 1.0
	v_fma_f32 v237, |v75|, s76, 1.0
	v_fma_f32 v255, |v77|, s76, 1.0
	v_pk_mul_f32 v[234:235], v[234:235], s[78:79] op_sel_hi:[1,0]
	v_pk_mul_f32 v[252:253], v[252:253], s[78:79] op_sel_hi:[1,0]
	v_rcp_f32_e32 v236, v236
	v_rcp_f32_e32 v254, v254
	v_rcp_f32_e32 v237, v237
	v_rcp_f32_e32 v255, v255
	v_exp_f32_e32 v234, v234
	v_exp_f32_e32 v252, v252
	v_exp_f32_e32 v235, v235
	v_exp_f32_e32 v253, v253
	v_pk_fma_f32 v[238:239], v[236:237], s[80:81], v[248:249] op_sel_hi:[1,0,1]
	v_pk_fma_f32 v[70:71], v[254:255], s[80:81], v[248:249] op_sel_hi:[1,0,1]
	v_pk_mul_f32 v[240:241], v[232:233], v[74:75] op_sel_hi:[0,1]
	v_pk_mul_f32 v[72:73], v[232:233], v[76:77] op_sel_hi:[0,1]
	v_pk_fma_f32 v[238:239], v[238:239], v[236:237], s[82:83] op_sel_hi:[1,1,0]
	v_pk_fma_f32 v[70:71], v[70:71], v[254:255], s[82:83] op_sel_hi:[1,1,0]
	v_pk_fma_f32 v[238:239], v[238:239], v[236:237], s[84:85] op_sel_hi:[1,1,0]
	v_pk_fma_f32 v[70:71], v[70:71], v[254:255], s[84:85] op_sel_hi:[1,1,0]
	v_pk_fma_f32 v[238:239], v[238:239], v[236:237], s[86:87] op_sel_hi:[1,1,0]
	v_pk_fma_f32 v[70:71], v[70:71], v[254:255], s[86:87] op_sel_hi:[1,1,0]
	v_pk_mul_f32 v[238:239], v[238:239], v[236:237]
	v_pk_mul_f32 v[70:71], v[70:71], v[254:255]
	v_pk_fma_f32 v[238:239], v[238:239], v[234:235], 1.0 op_sel_hi:[1,1,0] neg_lo:[1,0,0] neg_hi:[1,0,0]
	v_pk_fma_f32 v[70:71], v[70:71], v[252:253], 1.0 op_sel_hi:[1,1,0] neg_lo:[1,0,0] neg_hi:[1,0,0]
	v_fma_f32 v242, |v240|, v238, v240
	v_fma_f32 v0, |v72|, v70, v72
	v_fma_f32 v243, |v241|, v239, v241
	v_fma_f32 v1, |v73|, v71, v73
	v_cvt_pk_f16_f32 v244, v242, v243
	v_cvt_pk_f16_f32 v245, v0, v1
	v_pk_mul_f32 v[234:235], v[66:67], v[66:67]
	v_pk_mul_f32 v[252:253], v[68:69], v[68:69]
	v_fma_f32 v236, |v66|, s76, 1.0
	v_fma_f32 v254, |v68|, s76, 1.0
	v_fma_f32 v237, |v67|, s76, 1.0
	v_fma_f32 v255, |v69|, s76, 1.0
	v_pk_mul_f32 v[234:235], v[234:235], s[78:79] op_sel_hi:[1,0]
	v_pk_mul_f32 v[252:253], v[252:253], s[78:79] op_sel_hi:[1,0]
	v_rcp_f32_e32 v236, v236
	v_rcp_f32_e32 v254, v254
	v_rcp_f32_e32 v237, v237
	v_rcp_f32_e32 v255, v255
	v_exp_f32_e32 v234, v234
	v_exp_f32_e32 v252, v252
	v_exp_f32_e32 v235, v235
	v_exp_f32_e32 v253, v253
	v_pk_fma_f32 v[238:239], v[236:237], s[80:81], v[248:249] op_sel_hi:[1,0,1]
	v_pk_fma_f32 v[70:71], v[254:255], s[80:81], v[248:249] op_sel_hi:[1,0,1]
	v_pk_mul_f32 v[240:241], v[232:233], v[66:67] op_sel_hi:[0,1]
	v_pk_mul_f32 v[72:73], v[232:233], v[68:69] op_sel_hi:[0,1]
	v_pk_fma_f32 v[238:239], v[238:239], v[236:237], s[82:83] op_sel_hi:[1,1,0]
	v_pk_fma_f32 v[70:71], v[70:71], v[254:255], s[82:83] op_sel_hi:[1,1,0]
	v_pk_fma_f32 v[238:239], v[238:239], v[236:237], s[84:85] op_sel_hi:[1,1,0]
	v_pk_fma_f32 v[70:71], v[70:71], v[254:255], s[84:85] op_sel_hi:[1,1,0]
	v_pk_fma_f32 v[238:239], v[238:239], v[236:237], s[86:87] op_sel_hi:[1,1,0]
	v_pk_fma_f32 v[70:71], v[70:71], v[254:255], s[86:87] op_sel_hi:[1,1,0]
	v_pk_mul_f32 v[238:239], v[238:239], v[236:237]
	v_pk_mul_f32 v[70:71], v[70:71], v[254:255]
	v_pk_fma_f32 v[238:239], v[238:239], v[234:235], 1.0 op_sel_hi:[1,1,0] neg_lo:[1,0,0] neg_hi:[1,0,0]
	v_pk_fma_f32 v[70:71], v[70:71], v[252:253], 1.0 op_sel_hi:[1,1,0] neg_lo:[1,0,0] neg_hi:[1,0,0]
	v_fma_f32 v242, |v240|, v238, v240
	v_fma_f32 v0, |v72|, v70, v72
	v_fma_f32 v243, |v241|, v239, v241
	v_fma_f32 v1, |v73|, v71, v73
	v_cvt_pk_f16_f32 v246, v242, v243
	v_cvt_pk_f16_f32 v247, v0, v1
	v_cmp_lt_i32_e32 vcc, -1, v218
	s_nop 0
	v_permlane16_swap_b32_e32 v244, v246
	v_permlane16_swap_b32_e32 v245, v247
	s_and_saveexec_b64 s[10:11], vcc
	s_cbranch_execz .Lep_0
	v_mov_b32_e32 v250, v218
	v_mov_b32_e32 v251, 0
	v_lshlrev_b64 v[250:251], 10, v[250:251]
	v_lshl_add_u64 v[250:251], v[78:79], 0, v[250:251]
	global_store_dwordx4 v[250:251], v[244:247], off sc1
.Lep_0:
	s_or_b64 exec, exec, s[10:11]
	v_mul_f32_e32 v232, 0.5, v216
	v_pk_mul_f32 v[234:235], v[62:63], v[62:63]
	v_pk_mul_f32 v[252:253], v[64:65], v[64:65]
	v_fma_f32 v236, |v62|, s76, 1.0
	v_fma_f32 v254, |v64|, s76, 1.0
	v_fma_f32 v237, |v63|, s76, 1.0
	v_fma_f32 v255, |v65|, s76, 1.0
	v_pk_mul_f32 v[234:235], v[234:235], s[78:79] op_sel_hi:[1,0]
	v_pk_mul_f32 v[252:253], v[252:253], s[78:79] op_sel_hi:[1,0]
	v_rcp_f32_e32 v236, v236
	v_rcp_f32_e32 v254, v254
	v_rcp_f32_e32 v237, v237
	v_rcp_f32_e32 v255, v255
	v_exp_f32_e32 v234, v234
	v_exp_f32_e32 v252, v252
	v_exp_f32_e32 v235, v235
	v_exp_f32_e32 v253, v253
	v_pk_fma_f32 v[238:239], v[236:237], s[80:81], v[248:249] op_sel_hi:[1,0,1]
	v_pk_fma_f32 v[70:71], v[254:255], s[80:81], v[248:249] op_sel_hi:[1,0,1]
	v_pk_mul_f32 v[240:241], v[232:233], v[62:63] op_sel_hi:[0,1]
	v_pk_mul_f32 v[72:73], v[232:233], v[64:65] op_sel_hi:[0,1]
	v_pk_fma_f32 v[238:239], v[238:239], v[236:237], s[82:83] op_sel_hi:[1,1,0]
	v_pk_fma_f32 v[70:71], v[70:71], v[254:255], s[82:83] op_sel_hi:[1,1,0]
	v_pk_fma_f32 v[238:239], v[238:239], v[236:237], s[84:85] op_sel_hi:[1,1,0]
	v_pk_fma_f32 v[70:71], v[70:71], v[254:255], s[84:85] op_sel_hi:[1,1,0]
	v_pk_fma_f32 v[238:239], v[238:239], v[236:237], s[86:87] op_sel_hi:[1,1,0]
	v_pk_fma_f32 v[70:71], v[70:71], v[254:255], s[86:87] op_sel_hi:[1,1,0]
	v_pk_mul_f32 v[238:239], v[238:239], v[236:237]
	v_pk_mul_f32 v[70:71], v[70:71], v[254:255]
	v_pk_fma_f32 v[238:239], v[238:239], v[234:235], 1.0 op_sel_hi:[1,1,0] neg_lo:[1,0,0] neg_hi:[1,0,0]
	v_pk_fma_f32 v[70:71], v[70:71], v[252:253], 1.0 op_sel_hi:[1,1,0] neg_lo:[1,0,0] neg_hi:[1,0,0]
	v_fma_f32 v242, |v240|, v238, v240
	v_fma_f32 v0, |v72|, v70, v72
	v_fma_f32 v243, |v241|, v239, v241
	v_fma_f32 v1, |v73|, v71, v73
	v_cvt_pk_f16_f32 v244, v242, v243
	v_cvt_pk_f16_f32 v245, v0, v1
	v_pk_mul_f32 v[234:235], v[58:59], v[58:59]
	v_pk_mul_f32 v[252:253], v[60:61], v[60:61]
	v_fma_f32 v236, |v58|, s76, 1.0
	v_fma_f32 v254, |v60|, s76, 1.0
	v_fma_f32 v237, |v59|, s76, 1.0
	v_fma_f32 v255, |v61|, s76, 1.0
	v_pk_mul_f32 v[234:235], v[234:235], s[78:79] op_sel_hi:[1,0]
	v_pk_mul_f32 v[252:253], v[252:253], s[78:79] op_sel_hi:[1,0]
	v_rcp_f32_e32 v236, v236
	v_rcp_f32_e32 v254, v254
	v_rcp_f32_e32 v237, v237
	v_rcp_f32_e32 v255, v255
	v_exp_f32_e32 v234, v234
	v_exp_f32_e32 v252, v252
	v_exp_f32_e32 v235, v235
	v_exp_f32_e32 v253, v253
	v_pk_fma_f32 v[238:239], v[236:237], s[80:81], v[248:249] op_sel_hi:[1,0,1]
	v_pk_fma_f32 v[70:71], v[254:255], s[80:81], v[248:249] op_sel_hi:[1,0,1]
	v_pk_mul_f32 v[240:241], v[232:233], v[58:59] op_sel_hi:[0,1]
	v_pk_mul_f32 v[72:73], v[232:233], v[60:61] op_sel_hi:[0,1]
	v_pk_fma_f32 v[238:239], v[238:239], v[236:237], s[82:83] op_sel_hi:[1,1,0]
	v_pk_fma_f32 v[70:71], v[70:71], v[254:255], s[82:83] op_sel_hi:[1,1,0]
	v_pk_fma_f32 v[238:239], v[238:239], v[236:237], s[84:85] op_sel_hi:[1,1,0]
	v_pk_fma_f32 v[70:71], v[70:71], v[254:255], s[84:85] op_sel_hi:[1,1,0]
	v_pk_fma_f32 v[238:239], v[238:239], v[236:237], s[86:87] op_sel_hi:[1,1,0]
	v_pk_fma_f32 v[70:71], v[70:71], v[254:255], s[86:87] op_sel_hi:[1,1,0]
	v_pk_mul_f32 v[238:239], v[238:239], v[236:237]
	v_pk_mul_f32 v[70:71], v[70:71], v[254:255]
	v_pk_fma_f32 v[238:239], v[238:239], v[234:235], 1.0 op_sel_hi:[1,1,0] neg_lo:[1,0,0] neg_hi:[1,0,0]
	v_pk_fma_f32 v[70:71], v[70:71], v[252:253], 1.0 op_sel_hi:[1,1,0] neg_lo:[1,0,0] neg_hi:[1,0,0]
	v_fma_f32 v242, |v240|, v238, v240
	v_fma_f32 v0, |v72|, v70, v72
	v_fma_f32 v243, |v241|, v239, v241
	v_fma_f32 v1, |v73|, v71, v73
	v_cvt_pk_f16_f32 v246, v242, v243
	v_cvt_pk_f16_f32 v247, v0, v1
	v_cmp_lt_i32_e32 vcc, -1, v214
	s_nop 0
	v_permlane16_swap_b32_e32 v244, v246
	v_permlane16_swap_b32_e32 v245, v247
	s_and_saveexec_b64 s[10:11], vcc
	s_cbranch_execz .Lep_1
	v_mov_b32_e32 v250, v214
	v_mov_b32_e32 v251, 0
	v_lshlrev_b64 v[250:251], 10, v[250:251]
	v_lshl_add_u64 v[250:251], v[78:79], 0, v[250:251]
	global_store_dwordx4 v[250:251], v[244:247], off sc1
.Lep_1:
	s_or_b64 exec, exec, s[10:11]
	v_mul_f32_e32 v232, 0.5, v212
	v_pk_mul_f32 v[234:235], v[54:55], v[54:55]
	v_pk_mul_f32 v[252:253], v[56:57], v[56:57]
	v_fma_f32 v236, |v54|, s76, 1.0
	v_fma_f32 v254, |v56|, s76, 1.0
	v_fma_f32 v237, |v55|, s76, 1.0
	v_fma_f32 v255, |v57|, s76, 1.0
	v_pk_mul_f32 v[234:235], v[234:235], s[78:79] op_sel_hi:[1,0]
	v_pk_mul_f32 v[252:253], v[252:253], s[78:79] op_sel_hi:[1,0]
	v_rcp_f32_e32 v236, v236
	v_rcp_f32_e32 v254, v254
	v_rcp_f32_e32 v237, v237
	v_rcp_f32_e32 v255, v255
	v_exp_f32_e32 v234, v234
	v_exp_f32_e32 v252, v252
	v_exp_f32_e32 v235, v235
	v_exp_f32_e32 v253, v253
	v_pk_fma_f32 v[238:239], v[236:237], s[80:81], v[248:249] op_sel_hi:[1,0,1]
	v_pk_fma_f32 v[70:71], v[254:255], s[80:81], v[248:249] op_sel_hi:[1,0,1]
	v_pk_mul_f32 v[240:241], v[232:233], v[54:55] op_sel_hi:[0,1]
	v_pk_mul_f32 v[72:73], v[232:233], v[56:57] op_sel_hi:[0,1]
	v_pk_fma_f32 v[238:239], v[238:239], v[236:237], s[82:83] op_sel_hi:[1,1,0]
	v_pk_fma_f32 v[70:71], v[70:71], v[254:255], s[82:83] op_sel_hi:[1,1,0]
	v_pk_fma_f32 v[238:239], v[238:239], v[236:237], s[84:85] op_sel_hi:[1,1,0]
	v_pk_fma_f32 v[70:71], v[70:71], v[254:255], s[84:85] op_sel_hi:[1,1,0]
	v_pk_fma_f32 v[238:239], v[238:239], v[236:237], s[86:87] op_sel_hi:[1,1,0]
	v_pk_fma_f32 v[70:71], v[70:71], v[254:255], s[86:87] op_sel_hi:[1,1,0]
	v_pk_mul_f32 v[238:239], v[238:239], v[236:237]
	v_pk_mul_f32 v[70:71], v[70:71], v[254:255]
	v_pk_fma_f32 v[238:239], v[238:239], v[234:235], 1.0 op_sel_hi:[1,1,0] neg_lo:[1,0,0] neg_hi:[1,0,0]
	v_pk_fma_f32 v[70:71], v[70:71], v[252:253], 1.0 op_sel_hi:[1,1,0] neg_lo:[1,0,0] neg_hi:[1,0,0]
	v_fma_f32 v242, |v240|, v238, v240
	v_fma_f32 v0, |v72|, v70, v72
	v_fma_f32 v243, |v241|, v239, v241
	v_fma_f32 v1, |v73|, v71, v73
	v_cvt_pk_f16_f32 v244, v242, v243
	v_cvt_pk_f16_f32 v245, v0, v1
	v_pk_mul_f32 v[234:235], v[50:51], v[50:51]
	v_pk_mul_f32 v[252:253], v[52:53], v[52:53]
	v_fma_f32 v236, |v50|, s76, 1.0
	v_fma_f32 v254, |v52|, s76, 1.0
	v_fma_f32 v237, |v51|, s76, 1.0
	v_fma_f32 v255, |v53|, s76, 1.0
	v_pk_mul_f32 v[234:235], v[234:235], s[78:79] op_sel_hi:[1,0]
	v_pk_mul_f32 v[252:253], v[252:253], s[78:79] op_sel_hi:[1,0]
	v_rcp_f32_e32 v236, v236
	v_rcp_f32_e32 v254, v254
	v_rcp_f32_e32 v237, v237
	v_rcp_f32_e32 v255, v255
	v_exp_f32_e32 v234, v234
	v_exp_f32_e32 v252, v252
	v_exp_f32_e32 v235, v235
	v_exp_f32_e32 v253, v253
	v_pk_fma_f32 v[238:239], v[236:237], s[80:81], v[248:249] op_sel_hi:[1,0,1]
	v_pk_fma_f32 v[70:71], v[254:255], s[80:81], v[248:249] op_sel_hi:[1,0,1]
	v_pk_mul_f32 v[240:241], v[232:233], v[50:51] op_sel_hi:[0,1]
	v_pk_mul_f32 v[72:73], v[232:233], v[52:53] op_sel_hi:[0,1]
	v_pk_fma_f32 v[238:239], v[238:239], v[236:237], s[82:83] op_sel_hi:[1,1,0]
	v_pk_fma_f32 v[70:71], v[70:71], v[254:255], s[82:83] op_sel_hi:[1,1,0]
	v_pk_fma_f32 v[238:239], v[238:239], v[236:237], s[84:85] op_sel_hi:[1,1,0]
	v_pk_fma_f32 v[70:71], v[70:71], v[254:255], s[84:85] op_sel_hi:[1,1,0]
	v_pk_fma_f32 v[238:239], v[238:239], v[236:237], s[86:87] op_sel_hi:[1,1,0]
	v_pk_fma_f32 v[70:71], v[70:71], v[254:255], s[86:87] op_sel_hi:[1,1,0]
	v_pk_mul_f32 v[238:239], v[238:239], v[236:237]
	v_pk_mul_f32 v[70:71], v[70:71], v[254:255]
	v_pk_fma_f32 v[238:239], v[238:239], v[234:235], 1.0 op_sel_hi:[1,1,0] neg_lo:[1,0,0] neg_hi:[1,0,0]
	v_pk_fma_f32 v[70:71], v[70:71], v[252:253], 1.0 op_sel_hi:[1,1,0] neg_lo:[1,0,0] neg_hi:[1,0,0]
	v_fma_f32 v242, |v240|, v238, v240
	v_fma_f32 v0, |v72|, v70, v72
	v_fma_f32 v243, |v241|, v239, v241
	v_fma_f32 v1, |v73|, v71, v73
	v_cvt_pk_f16_f32 v246, v242, v243
	v_cvt_pk_f16_f32 v247, v0, v1
	v_cmp_lt_i32_e32 vcc, -1, v210
	s_nop 0
	v_permlane16_swap_b32_e32 v244, v246
	v_permlane16_swap_b32_e32 v245, v247
	s_and_saveexec_b64 s[10:11], vcc
	s_cbranch_execz .Lep_2
	v_mov_b32_e32 v250, v210
	v_mov_b32_e32 v251, 0
	v_lshlrev_b64 v[250:251], 10, v[250:251]
	v_lshl_add_u64 v[250:251], v[78:79], 0, v[250:251]
	global_store_dwordx4 v[250:251], v[244:247], off sc1
.Lep_2:
	s_or_b64 exec, exec, s[10:11]
	v_mul_f32_e32 v232, 0.5, v208
	v_pk_mul_f32 v[234:235], v[46:47], v[46:47]
	v_pk_mul_f32 v[252:253], v[48:49], v[48:49]
	v_fma_f32 v236, |v46|, s76, 1.0
	v_fma_f32 v254, |v48|, s76, 1.0
	v_fma_f32 v237, |v47|, s76, 1.0
	v_fma_f32 v255, |v49|, s76, 1.0
	v_pk_mul_f32 v[234:235], v[234:235], s[78:79] op_sel_hi:[1,0]
	v_pk_mul_f32 v[252:253], v[252:253], s[78:79] op_sel_hi:[1,0]
	v_rcp_f32_e32 v236, v236
	v_rcp_f32_e32 v254, v254
	v_rcp_f32_e32 v237, v237
	v_rcp_f32_e32 v255, v255
	v_exp_f32_e32 v234, v234
	v_exp_f32_e32 v252, v252
	v_exp_f32_e32 v235, v235
	v_exp_f32_e32 v253, v253
	v_pk_fma_f32 v[238:239], v[236:237], s[80:81], v[248:249] op_sel_hi:[1,0,1]
	v_pk_fma_f32 v[70:71], v[254:255], s[80:81], v[248:249] op_sel_hi:[1,0,1]
	v_pk_mul_f32 v[240:241], v[232:233], v[46:47] op_sel_hi:[0,1]
	v_pk_mul_f32 v[72:73], v[232:233], v[48:49] op_sel_hi:[0,1]
	v_pk_fma_f32 v[238:239], v[238:239], v[236:237], s[82:83] op_sel_hi:[1,1,0]
	v_pk_fma_f32 v[70:71], v[70:71], v[254:255], s[82:83] op_sel_hi:[1,1,0]
	v_pk_fma_f32 v[238:239], v[238:239], v[236:237], s[84:85] op_sel_hi:[1,1,0]
	v_pk_fma_f32 v[70:71], v[70:71], v[254:255], s[84:85] op_sel_hi:[1,1,0]
	v_pk_fma_f32 v[238:239], v[238:239], v[236:237], s[86:87] op_sel_hi:[1,1,0]
	v_pk_fma_f32 v[70:71], v[70:71], v[254:255], s[86:87] op_sel_hi:[1,1,0]
	v_pk_mul_f32 v[238:239], v[238:239], v[236:237]
	v_pk_mul_f32 v[70:71], v[70:71], v[254:255]
	v_pk_fma_f32 v[238:239], v[238:239], v[234:235], 1.0 op_sel_hi:[1,1,0] neg_lo:[1,0,0] neg_hi:[1,0,0]
	v_pk_fma_f32 v[70:71], v[70:71], v[252:253], 1.0 op_sel_hi:[1,1,0] neg_lo:[1,0,0] neg_hi:[1,0,0]
	v_fma_f32 v242, |v240|, v238, v240
	v_fma_f32 v0, |v72|, v70, v72
	v_fma_f32 v243, |v241|, v239, v241
	v_fma_f32 v1, |v73|, v71, v73
	v_cvt_pk_f16_f32 v244, v242, v243
	v_cvt_pk_f16_f32 v245, v0, v1
	v_pk_mul_f32 v[234:235], v[42:43], v[42:43]
	v_pk_mul_f32 v[252:253], v[44:45], v[44:45]
	v_fma_f32 v236, |v42|, s76, 1.0
	v_fma_f32 v254, |v44|, s76, 1.0
	v_fma_f32 v237, |v43|, s76, 1.0
	v_fma_f32 v255, |v45|, s76, 1.0
	v_pk_mul_f32 v[234:235], v[234:235], s[78:79] op_sel_hi:[1,0]
	v_pk_mul_f32 v[252:253], v[252:253], s[78:79] op_sel_hi:[1,0]
	v_rcp_f32_e32 v236, v236
	v_rcp_f32_e32 v254, v254
	v_rcp_f32_e32 v237, v237
	v_rcp_f32_e32 v255, v255
	v_exp_f32_e32 v234, v234
	v_exp_f32_e32 v252, v252
	v_exp_f32_e32 v235, v235
	v_exp_f32_e32 v253, v253
	v_pk_fma_f32 v[238:239], v[236:237], s[80:81], v[248:249] op_sel_hi:[1,0,1]
	v_pk_fma_f32 v[70:71], v[254:255], s[80:81], v[248:249] op_sel_hi:[1,0,1]
	v_pk_mul_f32 v[240:241], v[232:233], v[42:43] op_sel_hi:[0,1]
	v_pk_mul_f32 v[72:73], v[232:233], v[44:45] op_sel_hi:[0,1]
	v_pk_fma_f32 v[238:239], v[238:239], v[236:237], s[82:83] op_sel_hi:[1,1,0]
	v_pk_fma_f32 v[70:71], v[70:71], v[254:255], s[82:83] op_sel_hi:[1,1,0]
	v_pk_fma_f32 v[238:239], v[238:239], v[236:237], s[84:85] op_sel_hi:[1,1,0]
	v_pk_fma_f32 v[70:71], v[70:71], v[254:255], s[84:85] op_sel_hi:[1,1,0]
	v_pk_fma_f32 v[238:239], v[238:239], v[236:237], s[86:87] op_sel_hi:[1,1,0]
	v_pk_fma_f32 v[70:71], v[70:71], v[254:255], s[86:87] op_sel_hi:[1,1,0]
	v_pk_mul_f32 v[238:239], v[238:239], v[236:237]
	v_pk_mul_f32 v[70:71], v[70:71], v[254:255]
	v_pk_fma_f32 v[238:239], v[238:239], v[234:235], 1.0 op_sel_hi:[1,1,0] neg_lo:[1,0,0] neg_hi:[1,0,0]
	v_pk_fma_f32 v[70:71], v[70:71], v[252:253], 1.0 op_sel_hi:[1,1,0] neg_lo:[1,0,0] neg_hi:[1,0,0]
	v_fma_f32 v242, |v240|, v238, v240
	v_fma_f32 v0, |v72|, v70, v72
	v_fma_f32 v243, |v241|, v239, v241
	v_fma_f32 v1, |v73|, v71, v73
	v_cvt_pk_f16_f32 v246, v242, v243
	v_cvt_pk_f16_f32 v247, v0, v1
	v_cmp_lt_i32_e32 vcc, -1, v206
	s_nop 0
	v_permlane16_swap_b32_e32 v244, v246
	v_permlane16_swap_b32_e32 v245, v247
	s_and_saveexec_b64 s[10:11], vcc
	s_cbranch_execz .Lep_3
	v_mov_b32_e32 v250, v206
	v_mov_b32_e32 v251, 0
	v_lshlrev_b64 v[250:251], 10, v[250:251]
	v_lshl_add_u64 v[250:251], v[78:79], 0, v[250:251]
	global_store_dwordx4 v[250:251], v[244:247], off sc1
.Lep_3:
	s_or_b64 exec, exec, s[10:11]
	v_mul_f32_e32 v232, 0.5, v204
	v_pk_mul_f32 v[234:235], v[38:39], v[38:39]
	v_pk_mul_f32 v[252:253], v[40:41], v[40:41]
	v_fma_f32 v236, |v38|, s76, 1.0
	v_fma_f32 v254, |v40|, s76, 1.0
	v_fma_f32 v237, |v39|, s76, 1.0
	v_fma_f32 v255, |v41|, s76, 1.0
	v_pk_mul_f32 v[234:235], v[234:235], s[78:79] op_sel_hi:[1,0]
	v_pk_mul_f32 v[252:253], v[252:253], s[78:79] op_sel_hi:[1,0]
	v_rcp_f32_e32 v236, v236
	v_rcp_f32_e32 v254, v254
	v_rcp_f32_e32 v237, v237
	v_rcp_f32_e32 v255, v255
	v_exp_f32_e32 v234, v234
	v_exp_f32_e32 v252, v252
	v_exp_f32_e32 v235, v235
	v_exp_f32_e32 v253, v253
	v_pk_fma_f32 v[238:239], v[236:237], s[80:81], v[248:249] op_sel_hi:[1,0,1]
	v_pk_fma_f32 v[70:71], v[254:255], s[80:81], v[248:249] op_sel_hi:[1,0,1]
	v_pk_mul_f32 v[240:241], v[232:233], v[38:39] op_sel_hi:[0,1]
	v_pk_mul_f32 v[72:73], v[232:233], v[40:41] op_sel_hi:[0,1]
	v_pk_fma_f32 v[238:239], v[238:239], v[236:237], s[82:83] op_sel_hi:[1,1,0]
	v_pk_fma_f32 v[70:71], v[70:71], v[254:255], s[82:83] op_sel_hi:[1,1,0]
	v_pk_fma_f32 v[238:239], v[238:239], v[236:237], s[84:85] op_sel_hi:[1,1,0]
	v_pk_fma_f32 v[70:71], v[70:71], v[254:255], s[84:85] op_sel_hi:[1,1,0]
	v_pk_fma_f32 v[238:239], v[238:239], v[236:237], s[86:87] op_sel_hi:[1,1,0]
	v_pk_fma_f32 v[70:71], v[70:71], v[254:255], s[86:87] op_sel_hi:[1,1,0]
	v_pk_mul_f32 v[238:239], v[238:239], v[236:237]
	v_pk_mul_f32 v[70:71], v[70:71], v[254:255]
	v_pk_fma_f32 v[238:239], v[238:239], v[234:235], 1.0 op_sel_hi:[1,1,0] neg_lo:[1,0,0] neg_hi:[1,0,0]
	v_pk_fma_f32 v[70:71], v[70:71], v[252:253], 1.0 op_sel_hi:[1,1,0] neg_lo:[1,0,0] neg_hi:[1,0,0]
	v_fma_f32 v242, |v240|, v238, v240
	v_fma_f32 v0, |v72|, v70, v72
	v_fma_f32 v243, |v241|, v239, v241
	v_fma_f32 v1, |v73|, v71, v73
	v_cvt_pk_f16_f32 v244, v242, v243
	v_cvt_pk_f16_f32 v245, v0, v1
	v_pk_mul_f32 v[234:235], v[34:35], v[34:35]
	v_pk_mul_f32 v[252:253], v[36:37], v[36:37]
	v_fma_f32 v236, |v34|, s76, 1.0
	v_fma_f32 v254, |v36|, s76, 1.0
	v_fma_f32 v237, |v35|, s76, 1.0
	v_fma_f32 v255, |v37|, s76, 1.0
	v_pk_mul_f32 v[234:235], v[234:235], s[78:79] op_sel_hi:[1,0]
	v_pk_mul_f32 v[252:253], v[252:253], s[78:79] op_sel_hi:[1,0]
	v_rcp_f32_e32 v236, v236
	v_rcp_f32_e32 v254, v254
	v_rcp_f32_e32 v237, v237
	v_rcp_f32_e32 v255, v255
	v_exp_f32_e32 v234, v234
	v_exp_f32_e32 v252, v252
	v_exp_f32_e32 v235, v235
	v_exp_f32_e32 v253, v253
	v_pk_fma_f32 v[238:239], v[236:237], s[80:81], v[248:249] op_sel_hi:[1,0,1]
	v_pk_fma_f32 v[70:71], v[254:255], s[80:81], v[248:249] op_sel_hi:[1,0,1]
	v_pk_mul_f32 v[240:241], v[232:233], v[34:35] op_sel_hi:[0,1]
	v_pk_mul_f32 v[72:73], v[232:233], v[36:37] op_sel_hi:[0,1]
	v_pk_fma_f32 v[238:239], v[238:239], v[236:237], s[82:83] op_sel_hi:[1,1,0]
	v_pk_fma_f32 v[70:71], v[70:71], v[254:255], s[82:83] op_sel_hi:[1,1,0]
	v_pk_fma_f32 v[238:239], v[238:239], v[236:237], s[84:85] op_sel_hi:[1,1,0]
	v_pk_fma_f32 v[70:71], v[70:71], v[254:255], s[84:85] op_sel_hi:[1,1,0]
	v_pk_fma_f32 v[238:239], v[238:239], v[236:237], s[86:87] op_sel_hi:[1,1,0]
	v_pk_fma_f32 v[70:71], v[70:71], v[254:255], s[86:87] op_sel_hi:[1,1,0]
	v_pk_mul_f32 v[238:239], v[238:239], v[236:237]
	v_pk_mul_f32 v[70:71], v[70:71], v[254:255]
	v_pk_fma_f32 v[238:239], v[238:239], v[234:235], 1.0 op_sel_hi:[1,1,0] neg_lo:[1,0,0] neg_hi:[1,0,0]
	v_pk_fma_f32 v[70:71], v[70:71], v[252:253], 1.0 op_sel_hi:[1,1,0] neg_lo:[1,0,0] neg_hi:[1,0,0]
	v_fma_f32 v242, |v240|, v238, v240
	v_fma_f32 v0, |v72|, v70, v72
	v_fma_f32 v243, |v241|, v239, v241
	v_fma_f32 v1, |v73|, v71, v73
	v_cvt_pk_f16_f32 v246, v242, v243
	v_cvt_pk_f16_f32 v247, v0, v1
	v_cmp_lt_i32_e32 vcc, -1, v202
	s_nop 0
	v_permlane16_swap_b32_e32 v244, v246
	v_permlane16_swap_b32_e32 v245, v247
	s_and_saveexec_b64 s[10:11], vcc
	s_cbranch_execz .Lep_4
	v_mov_b32_e32 v250, v202
	v_mov_b32_e32 v251, 0
	v_lshlrev_b64 v[250:251], 10, v[250:251]
	v_lshl_add_u64 v[250:251], v[78:79], 0, v[250:251]
	global_store_dwordx4 v[250:251], v[244:247], off sc1
.Lep_4:
	s_or_b64 exec, exec, s[10:11]
	v_mul_f32_e32 v232, 0.5, v200
	v_pk_mul_f32 v[234:235], v[30:31], v[30:31]
	v_pk_mul_f32 v[252:253], v[32:33], v[32:33]
	v_fma_f32 v236, |v30|, s76, 1.0
	v_fma_f32 v254, |v32|, s76, 1.0
	v_fma_f32 v237, |v31|, s76, 1.0
	v_fma_f32 v255, |v33|, s76, 1.0
	v_pk_mul_f32 v[234:235], v[234:235], s[78:79] op_sel_hi:[1,0]
	v_pk_mul_f32 v[252:253], v[252:253], s[78:79] op_sel_hi:[1,0]
	v_rcp_f32_e32 v236, v236
	v_rcp_f32_e32 v254, v254
	v_rcp_f32_e32 v237, v237
	v_rcp_f32_e32 v255, v255
	v_exp_f32_e32 v234, v234
	v_exp_f32_e32 v252, v252
	v_exp_f32_e32 v235, v235
	v_exp_f32_e32 v253, v253
	v_pk_fma_f32 v[238:239], v[236:237], s[80:81], v[248:249] op_sel_hi:[1,0,1]
	v_pk_fma_f32 v[70:71], v[254:255], s[80:81], v[248:249] op_sel_hi:[1,0,1]
	v_pk_mul_f32 v[240:241], v[232:233], v[30:31] op_sel_hi:[0,1]
	v_pk_mul_f32 v[72:73], v[232:233], v[32:33] op_sel_hi:[0,1]
	v_pk_fma_f32 v[238:239], v[238:239], v[236:237], s[82:83] op_sel_hi:[1,1,0]
	v_pk_fma_f32 v[70:71], v[70:71], v[254:255], s[82:83] op_sel_hi:[1,1,0]
	v_pk_fma_f32 v[238:239], v[238:239], v[236:237], s[84:85] op_sel_hi:[1,1,0]
	v_pk_fma_f32 v[70:71], v[70:71], v[254:255], s[84:85] op_sel_hi:[1,1,0]
	v_pk_fma_f32 v[238:239], v[238:239], v[236:237], s[86:87] op_sel_hi:[1,1,0]
	v_pk_fma_f32 v[70:71], v[70:71], v[254:255], s[86:87] op_sel_hi:[1,1,0]
	v_pk_mul_f32 v[238:239], v[238:239], v[236:237]
	v_pk_mul_f32 v[70:71], v[70:71], v[254:255]
	v_pk_fma_f32 v[238:239], v[238:239], v[234:235], 1.0 op_sel_hi:[1,1,0] neg_lo:[1,0,0] neg_hi:[1,0,0]
	v_pk_fma_f32 v[70:71], v[70:71], v[252:253], 1.0 op_sel_hi:[1,1,0] neg_lo:[1,0,0] neg_hi:[1,0,0]
	v_fma_f32 v242, |v240|, v238, v240
	v_fma_f32 v0, |v72|, v70, v72
	v_fma_f32 v243, |v241|, v239, v241
	v_fma_f32 v1, |v73|, v71, v73
	v_cvt_pk_f16_f32 v244, v242, v243
	v_cvt_pk_f16_f32 v245, v0, v1
	v_pk_mul_f32 v[234:235], v[26:27], v[26:27]
	v_pk_mul_f32 v[252:253], v[28:29], v[28:29]
	v_fma_f32 v236, |v26|, s76, 1.0
	v_fma_f32 v254, |v28|, s76, 1.0
	v_fma_f32 v237, |v27|, s76, 1.0
	v_fma_f32 v255, |v29|, s76, 1.0
	v_pk_mul_f32 v[234:235], v[234:235], s[78:79] op_sel_hi:[1,0]
	v_pk_mul_f32 v[252:253], v[252:253], s[78:79] op_sel_hi:[1,0]
	v_rcp_f32_e32 v236, v236
	v_rcp_f32_e32 v254, v254
	v_rcp_f32_e32 v237, v237
	v_rcp_f32_e32 v255, v255
	v_exp_f32_e32 v234, v234
	v_exp_f32_e32 v252, v252
	v_exp_f32_e32 v235, v235
	v_exp_f32_e32 v253, v253
	v_pk_fma_f32 v[238:239], v[236:237], s[80:81], v[248:249] op_sel_hi:[1,0,1]
	v_pk_fma_f32 v[70:71], v[254:255], s[80:81], v[248:249] op_sel_hi:[1,0,1]
	v_pk_mul_f32 v[240:241], v[232:233], v[26:27] op_sel_hi:[0,1]
	v_pk_mul_f32 v[72:73], v[232:233], v[28:29] op_sel_hi:[0,1]
	v_pk_fma_f32 v[238:239], v[238:239], v[236:237], s[82:83] op_sel_hi:[1,1,0]
	v_pk_fma_f32 v[70:71], v[70:71], v[254:255], s[82:83] op_sel_hi:[1,1,0]
	v_pk_fma_f32 v[238:239], v[238:239], v[236:237], s[84:85] op_sel_hi:[1,1,0]
	v_pk_fma_f32 v[70:71], v[70:71], v[254:255], s[84:85] op_sel_hi:[1,1,0]
	v_pk_fma_f32 v[238:239], v[238:239], v[236:237], s[86:87] op_sel_hi:[1,1,0]
	v_pk_fma_f32 v[70:71], v[70:71], v[254:255], s[86:87] op_sel_hi:[1,1,0]
	v_pk_mul_f32 v[238:239], v[238:239], v[236:237]
	v_pk_mul_f32 v[70:71], v[70:71], v[254:255]
	v_pk_fma_f32 v[238:239], v[238:239], v[234:235], 1.0 op_sel_hi:[1,1,0] neg_lo:[1,0,0] neg_hi:[1,0,0]
	v_pk_fma_f32 v[70:71], v[70:71], v[252:253], 1.0 op_sel_hi:[1,1,0] neg_lo:[1,0,0] neg_hi:[1,0,0]
	v_fma_f32 v242, |v240|, v238, v240
	v_fma_f32 v0, |v72|, v70, v72
	v_fma_f32 v243, |v241|, v239, v241
	v_fma_f32 v1, |v73|, v71, v73
	v_cvt_pk_f16_f32 v246, v242, v243
	v_cvt_pk_f16_f32 v247, v0, v1
	v_cmp_lt_i32_e32 vcc, -1, v198
	s_nop 0
	v_permlane16_swap_b32_e32 v244, v246
	v_permlane16_swap_b32_e32 v245, v247
	s_and_saveexec_b64 s[10:11], vcc
	s_cbranch_execz .Lep_5
	v_mov_b32_e32 v250, v198
	v_mov_b32_e32 v251, 0
	v_lshlrev_b64 v[250:251], 10, v[250:251]
	v_lshl_add_u64 v[250:251], v[78:79], 0, v[250:251]
	global_store_dwordx4 v[250:251], v[244:247], off sc1
.Lep_5:
	s_or_b64 exec, exec, s[10:11]
	v_mul_f32_e32 v232, 0.5, v196
	v_pk_mul_f32 v[234:235], v[22:23], v[22:23]
	v_pk_mul_f32 v[252:253], v[24:25], v[24:25]
	v_fma_f32 v236, |v22|, s76, 1.0
	v_fma_f32 v254, |v24|, s76, 1.0
	v_fma_f32 v237, |v23|, s76, 1.0
	v_fma_f32 v255, |v25|, s76, 1.0
	v_pk_mul_f32 v[234:235], v[234:235], s[78:79] op_sel_hi:[1,0]
	v_pk_mul_f32 v[252:253], v[252:253], s[78:79] op_sel_hi:[1,0]
	v_rcp_f32_e32 v236, v236
	v_rcp_f32_e32 v254, v254
	v_rcp_f32_e32 v237, v237
	v_rcp_f32_e32 v255, v255
	v_exp_f32_e32 v234, v234
	v_exp_f32_e32 v252, v252
	v_exp_f32_e32 v235, v235
	v_exp_f32_e32 v253, v253
	v_pk_fma_f32 v[238:239], v[236:237], s[80:81], v[248:249] op_sel_hi:[1,0,1]
	v_pk_fma_f32 v[70:71], v[254:255], s[80:81], v[248:249] op_sel_hi:[1,0,1]
	v_pk_mul_f32 v[240:241], v[232:233], v[22:23] op_sel_hi:[0,1]
	v_pk_mul_f32 v[72:73], v[232:233], v[24:25] op_sel_hi:[0,1]
	v_pk_fma_f32 v[238:239], v[238:239], v[236:237], s[82:83] op_sel_hi:[1,1,0]
	v_pk_fma_f32 v[70:71], v[70:71], v[254:255], s[82:83] op_sel_hi:[1,1,0]
	v_pk_fma_f32 v[238:239], v[238:239], v[236:237], s[84:85] op_sel_hi:[1,1,0]
	v_pk_fma_f32 v[70:71], v[70:71], v[254:255], s[84:85] op_sel_hi:[1,1,0]
	v_pk_fma_f32 v[238:239], v[238:239], v[236:237], s[86:87] op_sel_hi:[1,1,0]
	v_pk_fma_f32 v[70:71], v[70:71], v[254:255], s[86:87] op_sel_hi:[1,1,0]
	v_pk_mul_f32 v[238:239], v[238:239], v[236:237]
	v_pk_mul_f32 v[70:71], v[70:71], v[254:255]
	v_pk_fma_f32 v[238:239], v[238:239], v[234:235], 1.0 op_sel_hi:[1,1,0] neg_lo:[1,0,0] neg_hi:[1,0,0]
	v_pk_fma_f32 v[70:71], v[70:71], v[252:253], 1.0 op_sel_hi:[1,1,0] neg_lo:[1,0,0] neg_hi:[1,0,0]
	v_fma_f32 v242, |v240|, v238, v240
	v_fma_f32 v0, |v72|, v70, v72
	v_fma_f32 v243, |v241|, v239, v241
	v_fma_f32 v1, |v73|, v71, v73
	v_cvt_pk_f16_f32 v244, v242, v243
	v_cvt_pk_f16_f32 v245, v0, v1
	v_pk_mul_f32 v[234:235], v[18:19], v[18:19]
	v_pk_mul_f32 v[252:253], v[20:21], v[20:21]
	v_fma_f32 v236, |v18|, s76, 1.0
	v_fma_f32 v254, |v20|, s76, 1.0
	v_fma_f32 v237, |v19|, s76, 1.0
	v_fma_f32 v255, |v21|, s76, 1.0
	v_pk_mul_f32 v[234:235], v[234:235], s[78:79] op_sel_hi:[1,0]
	v_pk_mul_f32 v[252:253], v[252:253], s[78:79] op_sel_hi:[1,0]
	v_rcp_f32_e32 v236, v236
	v_rcp_f32_e32 v254, v254
	v_rcp_f32_e32 v237, v237
	v_rcp_f32_e32 v255, v255
	v_exp_f32_e32 v234, v234
	v_exp_f32_e32 v252, v252
	v_exp_f32_e32 v235, v235
	v_exp_f32_e32 v253, v253
	v_pk_fma_f32 v[238:239], v[236:237], s[80:81], v[248:249] op_sel_hi:[1,0,1]
	v_pk_fma_f32 v[70:71], v[254:255], s[80:81], v[248:249] op_sel_hi:[1,0,1]
	v_pk_mul_f32 v[240:241], v[232:233], v[18:19] op_sel_hi:[0,1]
	v_pk_mul_f32 v[72:73], v[232:233], v[20:21] op_sel_hi:[0,1]
	v_pk_fma_f32 v[238:239], v[238:239], v[236:237], s[82:83] op_sel_hi:[1,1,0]
	v_pk_fma_f32 v[70:71], v[70:71], v[254:255], s[82:83] op_sel_hi:[1,1,0]
	v_pk_fma_f32 v[238:239], v[238:239], v[236:237], s[84:85] op_sel_hi:[1,1,0]
	v_pk_fma_f32 v[70:71], v[70:71], v[254:255], s[84:85] op_sel_hi:[1,1,0]
	v_pk_fma_f32 v[238:239], v[238:239], v[236:237], s[86:87] op_sel_hi:[1,1,0]
	v_pk_fma_f32 v[70:71], v[70:71], v[254:255], s[86:87] op_sel_hi:[1,1,0]
	v_pk_mul_f32 v[238:239], v[238:239], v[236:237]
	v_pk_mul_f32 v[70:71], v[70:71], v[254:255]
	v_pk_fma_f32 v[238:239], v[238:239], v[234:235], 1.0 op_sel_hi:[1,1,0] neg_lo:[1,0,0] neg_hi:[1,0,0]
	v_pk_fma_f32 v[70:71], v[70:71], v[252:253], 1.0 op_sel_hi:[1,1,0] neg_lo:[1,0,0] neg_hi:[1,0,0]
	v_fma_f32 v242, |v240|, v238, v240
	v_fma_f32 v0, |v72|, v70, v72
	v_fma_f32 v243, |v241|, v239, v241
	v_fma_f32 v1, |v73|, v71, v73
	v_cvt_pk_f16_f32 v246, v242, v243
	v_cvt_pk_f16_f32 v247, v0, v1
	v_cmp_lt_i32_e32 vcc, -1, v194
	s_nop 0
	v_permlane16_swap_b32_e32 v244, v246
	v_permlane16_swap_b32_e32 v245, v247
	s_and_saveexec_b64 s[10:11], vcc
	s_cbranch_execz .Lep_6
	v_mov_b32_e32 v250, v194
	v_mov_b32_e32 v251, 0
	v_lshlrev_b64 v[250:251], 10, v[250:251]
	v_lshl_add_u64 v[250:251], v[78:79], 0, v[250:251]
	global_store_dwordx4 v[250:251], v[244:247], off sc1
.Lep_6:
	s_or_b64 exec, exec, s[10:11]
	v_mul_f32_e32 v232, 0.5, v192
	v_pk_mul_f32 v[234:235], v[14:15], v[14:15]
	v_pk_mul_f32 v[252:253], v[16:17], v[16:17]
	v_fma_f32 v236, |v14|, s76, 1.0
	v_fma_f32 v254, |v16|, s76, 1.0
	v_fma_f32 v237, |v15|, s76, 1.0
	v_fma_f32 v255, |v17|, s76, 1.0
	v_pk_mul_f32 v[234:235], v[234:235], s[78:79] op_sel_hi:[1,0]
	v_pk_mul_f32 v[252:253], v[252:253], s[78:79] op_sel_hi:[1,0]
	v_rcp_f32_e32 v236, v236
	v_rcp_f32_e32 v254, v254
	v_rcp_f32_e32 v237, v237
	v_rcp_f32_e32 v255, v255
	v_exp_f32_e32 v234, v234
	v_exp_f32_e32 v252, v252
	v_exp_f32_e32 v235, v235
	v_exp_f32_e32 v253, v253
	v_pk_fma_f32 v[238:239], v[236:237], s[80:81], v[248:249] op_sel_hi:[1,0,1]
	v_pk_fma_f32 v[70:71], v[254:255], s[80:81], v[248:249] op_sel_hi:[1,0,1]
	v_pk_mul_f32 v[240:241], v[232:233], v[14:15] op_sel_hi:[0,1]
	v_pk_mul_f32 v[72:73], v[232:233], v[16:17] op_sel_hi:[0,1]
	v_pk_fma_f32 v[238:239], v[238:239], v[236:237], s[82:83] op_sel_hi:[1,1,0]
	v_pk_fma_f32 v[70:71], v[70:71], v[254:255], s[82:83] op_sel_hi:[1,1,0]
	v_pk_fma_f32 v[238:239], v[238:239], v[236:237], s[84:85] op_sel_hi:[1,1,0]
	v_pk_fma_f32 v[70:71], v[70:71], v[254:255], s[84:85] op_sel_hi:[1,1,0]
	v_pk_fma_f32 v[238:239], v[238:239], v[236:237], s[86:87] op_sel_hi:[1,1,0]
	v_pk_fma_f32 v[70:71], v[70:71], v[254:255], s[86:87] op_sel_hi:[1,1,0]
	v_pk_mul_f32 v[238:239], v[238:239], v[236:237]
	v_pk_mul_f32 v[70:71], v[70:71], v[254:255]
	v_pk_fma_f32 v[238:239], v[238:239], v[234:235], 1.0 op_sel_hi:[1,1,0] neg_lo:[1,0,0] neg_hi:[1,0,0]
	v_pk_fma_f32 v[70:71], v[70:71], v[252:253], 1.0 op_sel_hi:[1,1,0] neg_lo:[1,0,0] neg_hi:[1,0,0]
	v_fma_f32 v242, |v240|, v238, v240
	v_fma_f32 v0, |v72|, v70, v72
	v_fma_f32 v243, |v241|, v239, v241
	v_fma_f32 v1, |v73|, v71, v73
	v_cvt_pk_f16_f32 v244, v242, v243
	v_cvt_pk_f16_f32 v245, v0, v1
	v_pk_mul_f32 v[234:235], v[10:11], v[10:11]
	v_pk_mul_f32 v[252:253], v[12:13], v[12:13]
	v_fma_f32 v236, |v10|, s76, 1.0
	v_fma_f32 v254, |v12|, s76, 1.0
	v_fma_f32 v237, |v11|, s76, 1.0
	v_fma_f32 v255, |v13|, s76, 1.0
	v_pk_mul_f32 v[234:235], v[234:235], s[78:79] op_sel_hi:[1,0]
	v_pk_mul_f32 v[252:253], v[252:253], s[78:79] op_sel_hi:[1,0]
	v_rcp_f32_e32 v236, v236
	v_rcp_f32_e32 v254, v254
	v_rcp_f32_e32 v237, v237
	v_rcp_f32_e32 v255, v255
	v_exp_f32_e32 v234, v234
	v_exp_f32_e32 v252, v252
	v_exp_f32_e32 v235, v235
	v_exp_f32_e32 v253, v253
	v_pk_fma_f32 v[238:239], v[236:237], s[80:81], v[248:249] op_sel_hi:[1,0,1]
	v_pk_fma_f32 v[70:71], v[254:255], s[80:81], v[248:249] op_sel_hi:[1,0,1]
	v_pk_mul_f32 v[240:241], v[232:233], v[10:11] op_sel_hi:[0,1]
	v_pk_mul_f32 v[72:73], v[232:233], v[12:13] op_sel_hi:[0,1]
	v_pk_fma_f32 v[238:239], v[238:239], v[236:237], s[82:83] op_sel_hi:[1,1,0]
	v_pk_fma_f32 v[70:71], v[70:71], v[254:255], s[82:83] op_sel_hi:[1,1,0]
	v_pk_fma_f32 v[238:239], v[238:239], v[236:237], s[84:85] op_sel_hi:[1,1,0]
	v_pk_fma_f32 v[70:71], v[70:71], v[254:255], s[84:85] op_sel_hi:[1,1,0]
	v_pk_fma_f32 v[238:239], v[238:239], v[236:237], s[86:87] op_sel_hi:[1,1,0]
	v_pk_fma_f32 v[70:71], v[70:71], v[254:255], s[86:87] op_sel_hi:[1,1,0]
	v_pk_mul_f32 v[238:239], v[238:239], v[236:237]
	v_pk_mul_f32 v[70:71], v[70:71], v[254:255]
	v_pk_fma_f32 v[238:239], v[238:239], v[234:235], 1.0 op_sel_hi:[1,1,0] neg_lo:[1,0,0] neg_hi:[1,0,0]
	v_pk_fma_f32 v[70:71], v[70:71], v[252:253], 1.0 op_sel_hi:[1,1,0] neg_lo:[1,0,0] neg_hi:[1,0,0]
	v_fma_f32 v242, |v240|, v238, v240
	v_fma_f32 v0, |v72|, v70, v72
	v_fma_f32 v243, |v241|, v239, v241
	v_fma_f32 v1, |v73|, v71, v73
	v_cvt_pk_f16_f32 v246, v242, v243
	v_cvt_pk_f16_f32 v247, v0, v1
	v_cmp_lt_i32_e32 vcc, -1, v190
	s_nop 0
	v_permlane16_swap_b32_e32 v244, v246
	v_permlane16_swap_b32_e32 v245, v247
	s_and_saveexec_b64 s[10:11], vcc
	s_cbranch_execz .Lep_7
	v_mov_b32_e32 v250, v190
	v_mov_b32_e32 v251, 0
	v_lshlrev_b64 v[250:251], 10, v[250:251]
	v_lshl_add_u64 v[250:251], v[78:79], 0, v[250:251]
	global_store_dwordx4 v[250:251], v[244:247], off sc1
.Lep_7:
	s_or_b64 exec, exec, s[10:11]
	v_mul_f32_e32 v232, 0.5, v188
	v_pk_mul_f32 v[234:235], v[6:7], v[6:7]
	v_pk_mul_f32 v[252:253], v[8:9], v[8:9]
	v_fma_f32 v236, |v6|, s76, 1.0
	v_fma_f32 v254, |v8|, s76, 1.0
	v_fma_f32 v237, |v7|, s76, 1.0
	v_fma_f32 v255, |v9|, s76, 1.0
	v_pk_mul_f32 v[234:235], v[234:235], s[78:79] op_sel_hi:[1,0]
	v_pk_mul_f32 v[252:253], v[252:253], s[78:79] op_sel_hi:[1,0]
	v_rcp_f32_e32 v236, v236
	v_rcp_f32_e32 v254, v254
	v_rcp_f32_e32 v237, v237
	v_rcp_f32_e32 v255, v255
	v_exp_f32_e32 v234, v234
	v_exp_f32_e32 v252, v252
	v_exp_f32_e32 v235, v235
	v_exp_f32_e32 v253, v253
	v_pk_fma_f32 v[238:239], v[236:237], s[80:81], v[248:249] op_sel_hi:[1,0,1]
	v_pk_fma_f32 v[70:71], v[254:255], s[80:81], v[248:249] op_sel_hi:[1,0,1]
	v_pk_mul_f32 v[240:241], v[232:233], v[6:7] op_sel_hi:[0,1]
	v_pk_mul_f32 v[72:73], v[232:233], v[8:9] op_sel_hi:[0,1]
	v_pk_fma_f32 v[238:239], v[238:239], v[236:237], s[82:83] op_sel_hi:[1,1,0]
	v_pk_fma_f32 v[70:71], v[70:71], v[254:255], s[82:83] op_sel_hi:[1,1,0]
	v_pk_fma_f32 v[238:239], v[238:239], v[236:237], s[84:85] op_sel_hi:[1,1,0]
	v_pk_fma_f32 v[70:71], v[70:71], v[254:255], s[84:85] op_sel_hi:[1,1,0]
	v_pk_fma_f32 v[238:239], v[238:239], v[236:237], s[86:87] op_sel_hi:[1,1,0]
	v_pk_fma_f32 v[70:71], v[70:71], v[254:255], s[86:87] op_sel_hi:[1,1,0]
	v_pk_mul_f32 v[238:239], v[238:239], v[236:237]
	v_pk_mul_f32 v[70:71], v[70:71], v[254:255]
	v_pk_fma_f32 v[238:239], v[238:239], v[234:235], 1.0 op_sel_hi:[1,1,0] neg_lo:[1,0,0] neg_hi:[1,0,0]
	v_pk_fma_f32 v[70:71], v[70:71], v[252:253], 1.0 op_sel_hi:[1,1,0] neg_lo:[1,0,0] neg_hi:[1,0,0]
	v_fma_f32 v242, |v240|, v238, v240
	v_fma_f32 v0, |v72|, v70, v72
	v_fma_f32 v243, |v241|, v239, v241
	v_fma_f32 v1, |v73|, v71, v73
	v_cvt_pk_f16_f32 v244, v242, v243
	v_cvt_pk_f16_f32 v245, v0, v1
	v_pk_mul_f32 v[234:235], v[2:3], v[2:3]
	v_pk_mul_f32 v[252:253], v[4:5], v[4:5]
	v_fma_f32 v236, |v2|, s76, 1.0
	v_fma_f32 v254, |v4|, s76, 1.0
	v_fma_f32 v237, |v3|, s76, 1.0
	v_fma_f32 v255, |v5|, s76, 1.0
	v_pk_mul_f32 v[234:235], v[234:235], s[78:79] op_sel_hi:[1,0]
	v_pk_mul_f32 v[252:253], v[252:253], s[78:79] op_sel_hi:[1,0]
	v_rcp_f32_e32 v236, v236
	v_rcp_f32_e32 v254, v254
	v_rcp_f32_e32 v237, v237
	v_rcp_f32_e32 v255, v255
	v_exp_f32_e32 v234, v234
	v_exp_f32_e32 v252, v252
	v_exp_f32_e32 v235, v235
	v_exp_f32_e32 v253, v253
	v_pk_fma_f32 v[238:239], v[236:237], s[80:81], v[248:249] op_sel_hi:[1,0,1]
	v_pk_fma_f32 v[70:71], v[254:255], s[80:81], v[248:249] op_sel_hi:[1,0,1]
	v_pk_mul_f32 v[240:241], v[232:233], v[2:3] op_sel_hi:[0,1]
	v_pk_mul_f32 v[72:73], v[232:233], v[4:5] op_sel_hi:[0,1]
	v_pk_fma_f32 v[238:239], v[238:239], v[236:237], s[82:83] op_sel_hi:[1,1,0]
	v_pk_fma_f32 v[70:71], v[70:71], v[254:255], s[82:83] op_sel_hi:[1,1,0]
	v_pk_fma_f32 v[238:239], v[238:239], v[236:237], s[84:85] op_sel_hi:[1,1,0]
	v_pk_fma_f32 v[70:71], v[70:71], v[254:255], s[84:85] op_sel_hi:[1,1,0]
	v_pk_fma_f32 v[238:239], v[238:239], v[236:237], s[86:87] op_sel_hi:[1,1,0]
	v_pk_fma_f32 v[70:71], v[70:71], v[254:255], s[86:87] op_sel_hi:[1,1,0]
	v_pk_mul_f32 v[238:239], v[238:239], v[236:237]
	v_pk_mul_f32 v[70:71], v[70:71], v[254:255]
	v_pk_fma_f32 v[238:239], v[238:239], v[234:235], 1.0 op_sel_hi:[1,1,0] neg_lo:[1,0,0] neg_hi:[1,0,0]
	v_pk_fma_f32 v[70:71], v[70:71], v[252:253], 1.0 op_sel_hi:[1,1,0] neg_lo:[1,0,0] neg_hi:[1,0,0]
	v_fma_f32 v242, |v240|, v238, v240
	v_fma_f32 v0, |v72|, v70, v72
	v_fma_f32 v243, |v241|, v239, v241
	v_fma_f32 v1, |v73|, v71, v73
	v_cvt_pk_f16_f32 v246, v242, v243
	v_cvt_pk_f16_f32 v247, v0, v1
	v_cmp_lt_i32_e32 vcc, -1, v186
	s_nop 0
	v_permlane16_swap_b32_e32 v244, v246
	v_permlane16_swap_b32_e32 v245, v247
	s_and_saveexec_b64 s[10:11], vcc
	s_cbranch_execz .Lep_8
	v_mov_b32_e32 v250, v186
	v_mov_b32_e32 v251, 0
	v_lshlrev_b64 v[250:251], 10, v[250:251]
	v_lshl_add_u64 v[250:251], v[78:79], 0, v[250:251]
	global_store_dwordx4 v[250:251], v[244:247], off sc1
